# kpad
# speedup vs baseline: 1.0052x; 1.0052x over previous
.LBB3_9:
	v_readfirstlane_b32 s3, v196
	s_lshr_b32 s3, s3, 1
	v_and_b32_e32 v197, 31, v196
	s_and_b32 s3, s3, 0x7fffffe0
	v_or_b32_e32 v8, s3, v197
	v_mov_b32_e32 v9, 0
	v_lshlrev_b64 v[4:5], 8, v[8:9]
	v_lshrrev_b32_e32 v2, 1, v196
	v_lshl_add_u64 v[4:5], s[28:29], 0, v[4:5]
	v_and_b32_e32 v8, 16, v2
	s_lshl_b32 s3, s33, 6
	v_lshrrev_b32_e32 v201, 4, v196
	v_lshl_add_u64 v[10:11], v[4:5], 0, v[8:9]
	v_lshlrev_b32_e32 v2, 3, v196
	v_or_b32_e32 v5, s3, v201
	v_and_b32_e32 v4, 0x78, v2
	v_lshlrev_b32_e32 v8, 8, v5
	v_add_u32_e32 v210, 32, v201
	v_lshlrev_b32_e32 v198, 1, v4
	v_mov_b32_e32 v199, v9
	v_add_lshl_u32 v12, s3, v210, 8
	v_mov_b32_e32 v13, v9
	v_lshl_add_u64 v[14:15], s[26:27], 0, v[8:9]
	v_lshl_add_u64 v[14:15], v[14:15], 0, v[198:199]
	v_lshl_add_u64 v[16:17], s[26:27], 0, v[12:13]
	v_lshl_add_u64 v[16:17], v[16:17], 0, v[198:199]
	global_load_dwordx4 v[112:115], v[14:15], off
	global_load_dwordx4 v[116:119], v[16:17], off
	global_load_dwordx4 v[172:175], v[10:11], off
	global_load_dwordx4 v[168:171], v[10:11], off offset:32
	global_load_dwordx4 v[164:167], v[10:11], off offset:64
	global_load_dwordx4 v[148:151], v[10:11], off offset:96
	global_load_dwordx4 v[152:155], v[10:11], off offset:128
	global_load_dwordx4 v[156:159], v[10:11], off offset:160
	global_load_dwordx4 v[160:163], v[10:11], off offset:192
	global_load_dwordx4 v[144:147], v[10:11], off offset:224
	v_lshl_add_u64 v[8:9], s[24:25], 0, v[8:9]
	v_lshl_add_u64 v[8:9], v[8:9], 0, v[198:199]
	v_lshl_add_u64 v[10:11], s[24:25], 0, v[12:13]
	v_lshl_add_u64 v[10:11], v[10:11], 0, v[198:199]
	global_load_dwordx4 v[120:123], v[8:9], off
	global_load_dwordx4 v[124:127], v[10:11], off
	s_waitcnt vmcnt(13)
	v_or_b32_e32 v1, v6, v1
	s_movk_i32 s3, 0x70
	s_movk_i32 s4, 0x100
	s_waitcnt vmcnt(12)
	v_or3_b32 v1, v1, v7, v3
	v_lshlrev_b32_e32 v3, 8, v201
	v_lshl_add_u32 v5, v201, 4, v198
	v_add3_u32 v6, s4, v3, v5
	s_waitcnt vmcnt(0)
	v_cmp_ne_u32_e32 vcc, 0, v1
	s_waitcnt vmcnt(11)
	ds_write_b128 v6, v[112:115] offset:32768
	s_waitcnt vmcnt(10)
	ds_write_b128 v6, v[116:119] offset:41472
	s_waitcnt lgkmcnt(0)
	s_barrier
	s_load_dwordx2 s[6:7], s[0:1], 0x54
	s_load_dwordx2 s[4:5], s[0:1], 0x38
	v_cndmask_b32_e64 v1, 0, 1, vcc
	s_waitcnt lgkmcnt(0)
	s_lshr_b32 s1, s6, 16
	v_or_b32_dpp v1, v1, v1 row_shl:1 row_mask:0xf bank_mask:0xf bound_ctrl:1
	s_and_b32 s0, s6, 0xffff
	s_mul_i32 s6, s1, s0
	v_or_b32_dpp v1, v1, v1 row_shl:2 row_mask:0xf bank_mask:0xf bound_ctrl:1
	s_and_b32 s7, s7, 0xffff
	s_bfe_i32 s6, s6, 0x180000
	v_or_b32_dpp v1, v1, v1 row_shl:4 row_mask:0xf bank_mask:0xf bound_ctrl:1
	s_mul_i32 s6, s6, s7
	s_add_i32 s6, s6, 63
	v_or_b32_dpp v1, v1, v1 row_shl:8 row_mask:0xf bank_mask:0xf bound_ctrl:1
	s_bitcmp1_b32 exec_hi, 0
	s_nop 0
	v_mov_b32_dpp v7, v1 wave_shl:1 row_mask:0xf bank_mask:0xf bound_ctrl:1
	s_nop 1
	v_or_b32_dpp v1, v7, v1 row_mirror row_mask:0xf bank_mask:0xf bound_ctrl:1
	s_nop 0
	v_readlane_b32 s3, v1, 32
	v_readlane_b32 s8, v1, 0
	s_cselect_b32 s3, s3, 0
	s_or_b32 s3, s3, s8
	s_andn2_b32 s6, s6, 63
	s_cmp_eq_u32 s6, 64
	v_mov_b32_e32 v1, s3
	s_cbranch_scc1 .LBB3_16
	v_mbcnt_lo_u32_b32 v1, -1, 0
	v_mbcnt_hi_u32_b32 v6, -1, v1
	v_bfe_u32 v1, v0, 10, 10
	v_bfe_u32 v0, v0, 20, 10
	v_mad_u32_u24 v0, v0, s1, v1
	v_mad_u64_u32 v[0:1], s[0:1], v0, s0, v[196:197]
	v_lshrrev_b32_e32 v1, 6, v0
	v_or_b32_e32 v1, v6, v1
	v_cmp_eq_u32_e32 vcc, 0, v1
	s_and_saveexec_b64 s[0:1], vcc
	v_mov_b32_e32 v1, 0
	v_mov_b32_e32 v7, s3
	ds_write_b32 v1, v7
	s_or_b64 exec, exec, s[0:1]
	v_cmp_eq_u32_e32 vcc, 0, v6
	v_cmp_lt_u32_e64 s[0:1], 63, v0
	s_and_b64 s[6:7], s[0:1], vcc
	s_waitcnt lgkmcnt(0)
	s_barrier
	s_and_saveexec_b64 s[0:1], s[6:7]
	s_cbranch_execz .LBB3_15
	v_mbcnt_lo_u32_b32 v0, exec_lo, 0
	v_mbcnt_hi_u32_b32 v0, exec_hi, v0
	v_cmp_eq_u32_e32 vcc, 0, v0
	s_and_b64 exec, exec, vcc
	v_mov_b32_e32 v0, 0
	v_mov_b32_e32 v1, s3
	ds_or_b32 v0, v1

.LBB3_20:
	v_and_b32_e32 v1, 48, v201
	v_lshlrev_b32_e32 v7, 1, v201
	v_and_or_b32 v1, v7, 8, v1
	v_lshrrev_b32_e32 v7, 5, v196
	v_lshrrev_b32_e32 v1, 1, v1
	v_lshrrev_b32_e32 v4, 5, v4
	v_bfe_u32 v8, v196, 4, 2
	v_or_b32_e32 v1, v1, v4
	v_and_or_b32 v7, v7, 4, v8
	v_lshlrev_b32_e32 v1, 9, v1
	v_lshlrev_b32_e32 v7, 6, v7
	v_and_b32_e32 v8, 48, v198
	v_or3_b32 v9, v1, v7, v8
	v_and_b32_e32 v1, 0x70, v210
	v_lshlrev_b32_e32 v10, 1, v210
	v_and_or_b32 v1, v10, 8, v1
	v_lshrrev_b32_e32 v1, 1, v1
	v_or_b32_e32 v1, v1, v4
	v_lshlrev_b32_e32 v1, 9, v1
	v_or3_b32 v4, v1, v7, v8
	v_lshlrev_b32_e32 v1, 4, v196
	v_lshlrev_b32_e32 v7, 1, v196
	s_and_b64 s[0:1], exec, s[44:45]
	v_bfe_u32 v6, v196, 5, 1
	v_add_u32_e32 v3, v5, v3
	v_and_b32_e32 v5, 0xc0, v1
	v_and_b32_e32 v7, 32, v7
	v_and_b32_e32 v2, 0x118, v2
	s_cselect_b32 s11, 1, 2
	v_or3_b32 v2, v7, v5, v2
	s_movk_i32 s0, 0x100
	s_cmp_lg_u32 0x100, -1
	v_lshlrev_b32_e32 v5, 4, v6
	v_and_b32_e32 v1, 0x70, v1
	v_and_b32_e32 v0, 63, v196
	s_cselect_b32 s1, 0x100, 0
	v_xad_u32 v7, v5, v1, s0
	v_or_b32_e32 v8, 32, v5
	v_or_b32_e32 v10, 64, v5
	s_movk_i32 s2, 0x60
	v_or_b32_e32 v5, 0x60, v5
	v_lshlrev_b32_e32 v11, 5, v196
	v_and_b32_e32 v12, 28, v196
	v_lshlrev_b32_e32 v211, 2, v6
	v_add_u32_e32 v213, s1, v2
	v_xad_u32 v8, v8, v1, s0
	v_xad_u32 v10, v10, v1, s0
	v_xad_u32 v5, v5, v1, s0
	v_cmp_gt_u32_e64 s[0:1], 32, v0
	v_lshlrev_b32_e32 v0, 3, v6
	v_and_or_b32 v200, v11, s2, v12
	v_and_b32_e32 v11, 1, v196
	v_sub_u32_e32 v212, v197, v211
	v_lshlrev_b32_e32 v2, 8, v197
	v_mov_b32_e32 v1, 0
	v_cmp_eq_u32_e64 s[2:3], 0, v11
	v_and_b32_e32 v11, 2, v196
	v_lshlrev_b32_e32 v206, 1, v0
	v_mbcnt_lo_u32_b32 v0, -1, 0
	s_mov_b32 s9, 0
	v_cmp_eq_u32_e64 s[4:5], 0, v11
	v_lshlrev_b32_e32 v202, 10, v6
	v_mov_b32_e32 v203, v1
	v_mul_u32_u24_e32 v204, 0x8400, v6
	v_mov_b32_e32 v205, v1
	v_add_u32_e32 v214, 0xffffff45, v212
	v_add_u32_e32 v215, 0x100, v9
	v_add_u32_e32 v216, 0x100, v4
	s_mov_b32 s20, 0x41000000
	s_mov_b32 s10, 0x3e0293ee
	v_lshlrev_b32_e32 v218, 4, v197
	v_lshl_add_u32 v217, v6, 4, v2
	v_add_u32_e32 v217, v217, v218
	v_add_u32_e32 v217, 0x100, v217
	v_mov_b32_e32 v221, 0xff800000
	v_add_u32_e32 v222, 0x100, v3
	v_mov_b32_e32 v223, 0xf149f2ca
	v_mbcnt_hi_u32_b32 v224, -1, v0
	s_mov_b32 s53, 0
	s_branch .LBB3_23

.LBB3_25:
	s_and_b64 s[6:7], s[12:13], exec
	s_cselect_b32 s55, s48, s50
	s_lshr_b32 s6, s59, 1
	s_and_b32 s8, s6, 0x7fffffe0
	s_add_i32 s55, s55, s8
	v_add_u32_e32 v227, s55, v212
	ds_read_b128 v[2:5], v217 offset:32768
	ds_read_b128 v[34:37], v217 offset:32896
	s_or_b32 s6, s60, 63
	s_cmp_le_u32 s6, s55
	s_cselect_b64 s[6:7], -1, 0
	s_waitcnt lgkmcnt(1)
	v_mfma_f32_32x32x16_bf16 v[18:33], v[2:5], v[172:175], 0
	ds_read_b128 v[2:5], v217 offset:41472
	ds_read_b128 v[38:41], v217 offset:41600
	ds_read_b128 v[42:45], v217 offset:32800
	ds_read_b128 v[46:49], v217 offset:32928
	s_sub_i32 s56, s55, s21
	s_add_i32 s56, s56, 31
	s_cmp_gt_i32 s60, s56
	s_cselect_b64 s[62:63], -1, 0
	s_and_b64 s[6:7], s[6:7], s[62:63]
	s_waitcnt lgkmcnt(3)
	v_mfma_f32_32x32x16_bf16 v[2:17], v[2:5], v[172:175], 0
	s_and_b64 vcc, exec, s[6:7]
	s_waitcnt lgkmcnt(1)
	v_mfma_f32_32x32x16_bf16 v[18:33], v[42:45], v[168:171], v[18:33]
	ds_read_b128 v[42:45], v217 offset:41504
	ds_read_b128 v[50:53], v217 offset:41632
	s_waitcnt lgkmcnt(1)
	v_mfma_f32_32x32x16_bf16 v[2:17], v[42:45], v[168:171], v[2:17]
	ds_read_b128 v[42:45], v217 offset:32832
	ds_read_b128 v[54:57], v217 offset:32960
	s_waitcnt lgkmcnt(1)
	v_mfma_f32_32x32x16_bf16 v[18:33], v[42:45], v[164:167], v[18:33]
	ds_read_b128 v[42:45], v217 offset:41536
	ds_read_b128 v[58:61], v217 offset:41664
	s_waitcnt lgkmcnt(1)
	v_mfma_f32_32x32x16_bf16 v[2:17], v[42:45], v[164:167], v[2:17]
	ds_read_b128 v[42:45], v217 offset:32864
	ds_read_b128 v[62:65], v217 offset:32992
	s_waitcnt lgkmcnt(1)
	v_mfma_f32_32x32x16_bf16 v[18:33], v[42:45], v[148:151], v[18:33]
	ds_read_b128 v[42:45], v217 offset:41568
	ds_read_b128 v[66:69], v217 offset:41696
	s_waitcnt lgkmcnt(1)
	v_mfma_f32_32x32x16_bf16 v[2:17], v[42:45], v[148:151], v[2:17]
	v_mfma_f32_32x32x16_bf16 v[18:33], v[34:37], v[152:155], v[18:33]
	v_mfma_f32_32x32x16_bf16 v[2:17], v[38:41], v[152:155], v[2:17]
	v_mfma_f32_32x32x16_bf16 v[18:33], v[46:49], v[156:159], v[18:33]
	v_mfma_f32_32x32x16_bf16 v[2:17], v[50:53], v[156:159], v[2:17]
	v_mfma_f32_32x32x16_bf16 v[18:33], v[54:57], v[160:163], v[18:33]
	v_mfma_f32_32x32x16_bf16 v[2:17], v[58:61], v[160:163], v[2:17]
	v_mfma_f32_32x32x16_bf16 v[18:33], v[62:65], v[144:147], v[18:33]
	s_waitcnt lgkmcnt(0)
	v_mfma_f32_32x32x16_bf16 v[2:17], v[66:69], v[144:147], v[2:17]
	s_cbranch_vccnz .LBB3_27
	v_subrev_u32_e32 v0, s60, v227
	v_cmp_gt_u32_e32 vcc, s21, v0
	v_subrev_u32_e32 v34, 32, v0
	s_nop 5
	v_cndmask_b32_e32 v18, v221, v18, vcc
	v_cmp_gt_u32_e32 vcc, s21, v34
	v_add_u32_e32 v34, -1, v0
	s_nop 0
	v_cndmask_b32_e32 v2, v221, v2, vcc
	v_cmp_gt_u32_e32 vcc, s21, v34
	v_subrev_u32_e32 v34, 33, v0
	s_nop 0
	v_cndmask_b32_e32 v19, v221, v19, vcc
	v_cmp_gt_u32_e32 vcc, s21, v34
	v_add_u32_e32 v34, -2, v0
	s_nop 0
	v_cndmask_b32_e32 v3, v221, v3, vcc
	v_cmp_gt_u32_e32 vcc, s21, v34
	v_subrev_u32_e32 v34, 34, v0
	s_nop 0
	v_cndmask_b32_e32 v20, v221, v20, vcc
	v_cmp_gt_u32_e32 vcc, s21, v34
	v_add_u32_e32 v34, -3, v0
	s_nop 0
	v_cndmask_b32_e32 v4, v221, v4, vcc
	v_cmp_gt_u32_e32 vcc, s21, v34
	v_subrev_u32_e32 v34, 35, v0
	s_nop 0
	v_cndmask_b32_e32 v21, v221, v21, vcc
	v_cmp_gt_u32_e32 vcc, s21, v34
	v_add_u32_e32 v34, -8, v0
	s_nop 0
	v_cndmask_b32_e32 v5, v221, v5, vcc
	v_cmp_gt_u32_e32 vcc, s21, v34
	v_subrev_u32_e32 v34, 40, v0
	s_nop 0
	v_cndmask_b32_e32 v22, v221, v22, vcc
	v_cmp_gt_u32_e32 vcc, s21, v34
	v_add_u32_e32 v34, -9, v0
	s_nop 0
	v_cndmask_b32_e32 v6, v221, v6, vcc
	v_cmp_gt_u32_e32 vcc, s21, v34
	v_subrev_u32_e32 v34, 41, v0
	s_nop 0
	v_cndmask_b32_e32 v23, v221, v23, vcc
	v_cmp_gt_u32_e32 vcc, s21, v34
	v_add_u32_e32 v34, -10, v0
	s_nop 0
	v_cndmask_b32_e32 v7, v221, v7, vcc
	v_cmp_gt_u32_e32 vcc, s21, v34
	v_subrev_u32_e32 v34, 42, v0
	s_nop 0
	v_cndmask_b32_e32 v24, v221, v24, vcc
	v_cmp_gt_u32_e32 vcc, s21, v34
	v_add_u32_e32 v34, -11, v0
	s_nop 0
	v_cndmask_b32_e32 v8, v221, v8, vcc
	v_cmp_gt_u32_e32 vcc, s21, v34
	v_subrev_u32_e32 v34, 43, v0
	s_nop 0
	v_cndmask_b32_e32 v25, v221, v25, vcc
	v_cmp_gt_u32_e32 vcc, s21, v34
	v_add_u32_e32 v34, -16, v0
	s_nop 0
	v_cndmask_b32_e32 v9, v221, v9, vcc
	v_cmp_gt_u32_e32 vcc, s21, v34
	v_subrev_u32_e32 v34, 48, v0
	s_nop 0
	v_cndmask_b32_e32 v26, v221, v26, vcc
	v_cmp_gt_u32_e32 vcc, s21, v34
	v_subrev_u32_e32 v34, 17, v0
	s_nop 0
	v_cndmask_b32_e32 v10, v221, v10, vcc
	v_cmp_gt_u32_e32 vcc, s21, v34
	v_subrev_u32_e32 v34, 49, v0
	s_nop 0
	v_cndmask_b32_e32 v27, v221, v27, vcc
	v_cmp_gt_u32_e32 vcc, s21, v34
	v_subrev_u32_e32 v34, 18, v0
	s_nop 0
	v_cndmask_b32_e32 v11, v221, v11, vcc
	v_cmp_gt_u32_e32 vcc, s21, v34
	v_subrev_u32_e32 v34, 50, v0
	s_nop 0
	v_cndmask_b32_e32 v28, v221, v28, vcc
	v_cmp_gt_u32_e32 vcc, s21, v34
	v_subrev_u32_e32 v34, 19, v0
	s_nop 0
	v_cndmask_b32_e32 v12, v221, v12, vcc
	v_cmp_gt_u32_e32 vcc, s21, v34
	v_subrev_u32_e32 v34, 51, v0
	s_nop 0
	v_cndmask_b32_e32 v29, v221, v29, vcc
	v_cmp_gt_u32_e32 vcc, s21, v34
	v_subrev_u32_e32 v34, 24, v0
	s_nop 0
	v_cndmask_b32_e32 v13, v221, v13, vcc
	v_cmp_gt_u32_e32 vcc, s21, v34
	v_subrev_u32_e32 v34, 56, v0
	s_nop 0
	v_cndmask_b32_e32 v30, v221, v30, vcc
	v_cmp_gt_u32_e32 vcc, s21, v34
	v_subrev_u32_e32 v34, 25, v0
	s_nop 0
	v_cndmask_b32_e32 v14, v221, v14, vcc
	v_cmp_gt_u32_e32 vcc, s21, v34
	v_subrev_u32_e32 v34, 57, v0
	s_nop 0
	v_cndmask_b32_e32 v31, v221, v31, vcc
	v_cmp_gt_u32_e32 vcc, s21, v34
	v_subrev_u32_e32 v34, 26, v0
	s_nop 0
	v_cndmask_b32_e32 v15, v221, v15, vcc
	v_cmp_gt_u32_e32 vcc, s21, v34
	v_subrev_u32_e32 v34, 58, v0
	s_nop 0
	v_cndmask_b32_e32 v32, v221, v32, vcc
	v_cmp_gt_u32_e32 vcc, s21, v34
	v_subrev_u32_e32 v34, 27, v0
	v_subrev_u32_e32 v0, 59, v0
	v_cndmask_b32_e32 v16, v221, v16, vcc
	v_cmp_gt_u32_e32 vcc, s21, v34
	s_nop 1
	v_cndmask_b32_e32 v33, v221, v33, vcc
	v_cmp_gt_u32_e32 vcc, s21, v0
	s_nop 1
	v_cndmask_b32_e32 v17, v221, v17, vcc
.LBB3_27:
	s_nop 8
	v_max_f32_e32 v0, v19, v19
	v_max_f32_e32 v34, v18, v18
	v_max_f32_e32 v0, v34, v0
	v_max3_f32 v0, v0, v20, v21
	v_max3_f32 v0, v0, v22, v23
	v_max3_f32 v0, v0, v24, v25
	v_max3_f32 v0, v0, v26, v27
	v_max3_f32 v0, v0, v28, v29
	v_max3_f32 v0, v0, v30, v31
	v_max3_f32 v0, v0, v32, v33
	v_max3_f32 v0, v0, v2, v3
	v_max3_f32 v0, v0, v4, v5
	v_max3_f32 v0, v0, v6, v7
	v_max3_f32 v0, v0, v8, v9
	v_max3_f32 v0, v0, v10, v11
	v_max3_f32 v0, v0, v12, v13
	v_max3_f32 v0, v0, v14, v15
	v_max3_f32 v0, v0, v16, v17
	v_mov_b32_e32 v34, v0
	s_nop 1
	v_permlane32_swap_b32_e32 v0, v34
	v_max_f32_e32 v34, v34, v34
	v_max_f32_e32 v0, v0, v0
	v_max_f32_e32 v0, v0, v34
	v_add_f32_e32 v34, 0x7149f2ca, v0
	v_mul_f32_e32 v34, 0x3db504f3, v34
	v_cmp_ge_f32_e32 vcc, s20, v34
	s_cmp_eq_u64 vcc, exec
	s_cselect_b64 s[6:7], -1, 0
	s_andn2_b64 vcc, exec, s[46:47]
	s_cbranch_vccnz .LBB3_29
	s_waitcnt vmcnt(0)
	s_waitcnt vmcnt(3)
	ds_write_b128 v215, v[120:123] offset:16384
	s_waitcnt vmcnt(2)
	ds_write_b128 v216, v[124:127] offset:16384
	s_waitcnt vmcnt(1)
	ds_write_b128 v222, v[112:115] offset:50176
	s_waitcnt vmcnt(0)
	ds_write_b128 v222, v[116:119] offset:58880
.LBB3_29:
	v_max_f32_e32 v34, 0xf149f2ca, v0
	v_cndmask_b32_e64 v180, v34, v223, s[6:7]
	v_mul_f32_e32 v0, 0xbe0293ee, v180
	v_fmamk_f32 v18, v18, 0x3e0293ee, v0
	v_exp_f32_e32 v191, v18
	v_sub_f32_e32 v18, 0xf149f2ca, v34
	v_mul_f32_e32 v18, 0x3e0293ee, v18
	v_exp_f32_e32 v18, v18
	v_fmamk_f32 v19, v19, 0x3e0293ee, v0
	v_fmamk_f32 v20, v20, 0x3e0293ee, v0
	v_fmamk_f32 v21, v21, 0x3e0293ee, v0
	v_fmamk_f32 v22, v22, 0x3e0293ee, v0
	v_fmamk_f32 v23, v23, 0x3e0293ee, v0
	v_fmamk_f32 v24, v24, 0x3e0293ee, v0
	v_fmamk_f32 v25, v25, 0x3e0293ee, v0
	v_fmamk_f32 v26, v26, 0x3e0293ee, v0
	v_fmamk_f32 v27, v27, 0x3e0293ee, v0
	v_fmamk_f32 v28, v28, 0x3e0293ee, v0
	v_fmamk_f32 v29, v29, 0x3e0293ee, v0
	v_fmamk_f32 v30, v30, 0x3e0293ee, v0
	v_fmamk_f32 v31, v31, 0x3e0293ee, v0
	v_fmamk_f32 v32, v32, 0x3e0293ee, v0
	v_fmamk_f32 v33, v33, 0x3e0293ee, v0
	v_cndmask_b32_e64 v228, v18, 1.0, s[6:7]
	s_and_b32 s6, s59, 0x3fffffc0
	v_exp_f32_e32 v193, v19
	v_exp_f32_e32 v189, v20
	v_exp_f32_e32 v192, v21
	v_exp_f32_e32 v188, v22
	v_exp_f32_e32 v190, v23
	v_exp_f32_e32 v186, v24
	v_exp_f32_e32 v187, v25
	v_exp_f32_e32 v179, v26
	v_exp_f32_e32 v184, v27
	v_exp_f32_e32 v177, v28
	v_exp_f32_e32 v182, v29
	v_exp_f32_e32 v176, v30
	v_exp_f32_e32 v185, v31
	v_exp_f32_e32 v178, v32
	v_exp_f32_e32 v183, v33
	s_lshl_b32 s6, s6, 2
	s_addk_i32 s6, 0x100
	s_add_i32 s6, s6, 0x10800
	v_pk_fma_f32 v[128:129], v[16:17], s[10:11], v[0:1] op_sel_hi:[1,0,0]
	v_pk_fma_f32 v[130:131], v[14:15], s[10:11], v[0:1] op_sel_hi:[1,0,0]
	v_pk_fma_f32 v[132:133], v[12:13], s[10:11], v[0:1] op_sel_hi:[1,0,0]
	v_pk_fma_f32 v[134:135], v[10:11], s[10:11], v[0:1] op_sel_hi:[1,0,0]
	v_pk_fma_f32 v[136:137], v[8:9], s[10:11], v[0:1] op_sel_hi:[1,0,0]
	v_pk_fma_f32 v[138:139], v[6:7], s[10:11], v[0:1] op_sel_hi:[1,0,0]
	v_pk_fma_f32 v[140:141], v[4:5], s[10:11], v[0:1] op_sel_hi:[1,0,0]
	v_pk_fma_f32 v[142:143], v[2:3], s[10:11], v[0:1] op_sel_hi:[1,0,0]
	s_cmp_lt_i32 s58, 3
	v_lshl_add_u32 v226, v197, 2, s6
	v_lshl_add_u32 v225, v211, 2, s6
	s_waitcnt lgkmcnt(0)
	s_barrier
	s_cbranch_scc1 .LBB3_48
	v_mov_b32_e32 v199, v1
	v_add_u32_e32 v0, s55, v214
	v_mov_b32_e32 v229, 0
	v_lshl_add_u64 v[14:15], s[44:45], 0, v[198:199]
	v_lshl_add_u64 v[208:209], s[14:15], 0, v[198:199]
	s_mov_b32 s59, 2
	v_subrev_u32_e32 v0, s60, v0
	s_addk_i32 s60, 0x7f
	v_mov_b32_e32 v64, 0
	v_mov_b32_e32 v65, v229
	v_mov_b32_e32 v66, v229
	v_mov_b32_e32 v67, v229
	v_mov_b32_e32 v68, v229
	v_mov_b32_e32 v69, v229
	v_mov_b32_e32 v70, v229
	v_mov_b32_e32 v71, v229
	v_mov_b32_e32 v72, v229
	v_mov_b32_e32 v73, v229
	v_mov_b32_e32 v74, v229
	v_mov_b32_e32 v75, v229
	v_mov_b32_e32 v76, v229
	v_mov_b32_e32 v77, v229
	v_mov_b32_e32 v78, v229
	v_mov_b32_e32 v79, v229
	v_mov_b32_e32 v48, 0
	v_mov_b32_e32 v49, v229
	v_mov_b32_e32 v50, v229
	v_mov_b32_e32 v51, v229
	v_mov_b32_e32 v52, v229
	v_mov_b32_e32 v53, v229
	v_mov_b32_e32 v54, v229
	v_mov_b32_e32 v55, v229
	v_mov_b32_e32 v56, v229
	v_mov_b32_e32 v57, v229
	v_mov_b32_e32 v58, v229
	v_mov_b32_e32 v59, v229
	v_mov_b32_e32 v60, v229
	v_mov_b32_e32 v61, v229
	v_mov_b32_e32 v62, v229
	v_mov_b32_e32 v63, v229
	v_mov_b32_e32 v32, 0
	v_mov_b32_e32 v33, v229
	v_mov_b32_e32 v34, v229
	v_mov_b32_e32 v35, v229
	v_mov_b32_e32 v36, v229
	v_mov_b32_e32 v37, v229
	v_mov_b32_e32 v38, v229
	v_mov_b32_e32 v39, v229
	v_mov_b32_e32 v40, v229
	v_mov_b32_e32 v41, v229
	v_mov_b32_e32 v42, v229
	v_mov_b32_e32 v43, v229
	v_mov_b32_e32 v44, v229
	v_mov_b32_e32 v45, v229
	v_mov_b32_e32 v46, v229
	v_mov_b32_e32 v47, v229
	v_mov_b32_e32 v16, 0
	v_mov_b32_e32 v17, v229
	v_mov_b32_e32 v18, v229
	v_mov_b32_e32 v19, v229
	v_mov_b32_e32 v20, v229
	v_mov_b32_e32 v21, v229
	v_mov_b32_e32 v22, v229
	v_mov_b32_e32 v23, v229
	v_mov_b32_e32 v24, v229
	v_mov_b32_e32 v25, v229
	v_mov_b32_e32 v26, v229
	v_mov_b32_e32 v27, v229
	v_mov_b32_e32 v28, v229
	v_mov_b32_e32 v29, v229
	v_mov_b32_e32 v30, v229
	v_mov_b32_e32 v31, v229
	s_branch .LBB3_33

.LBB3_33:
	ds_read_b128 v[2:5], v217 offset:50176
	ds_read_b128 v[6:9], v217 offset:50304
	v_exp_f32_e32 v142, v142
	v_exp_f32_e32 v143, v143
	v_exp_f32_e32 v140, v140
	s_waitcnt vmcnt(1) lgkmcnt(1)
	v_mfma_f32_32x32x16_bf16 v[100:115], v[2:5], v[172:175], 0
	ds_read_b128 v[2:5], v217 offset:58880
	ds_read_b128 v[10:13], v217 offset:59008
	v_exp_f32_e32 v141, v141
	v_exp_f32_e32 v138, v138
	v_exp_f32_e32 v134, v134
	v_exp_f32_e32 v135, v135
	v_exp_f32_e32 v132, v132
	v_exp_f32_e32 v133, v133
	s_waitcnt lgkmcnt(1)
	v_mfma_f32_32x32x16_bf16 v[84:99], v[2:5], v[172:175], 0
	ds_read_b128 v[2:5], v217 offset:50208
	ds_read_b128 v[80:83], v217 offset:58912
	s_waitcnt vmcnt(0)
	ds_read_b128 v[116:119], v217 offset:50336
	v_exp_f32_e32 v130, v130
	v_exp_f32_e32 v131, v131
	v_exp_f32_e32 v128, v128
	v_exp_f32_e32 v129, v129
	s_sub_i32 s6, s60, 63
	s_waitcnt lgkmcnt(2)
	v_mfma_f32_32x32x16_bf16 v[100:115], v[2:5], v[168:171], v[100:115]
	ds_read_b128 v[2:5], v217 offset:59040
	ds_read_b128 v[120:123], v217 offset:50240
	ds_read_b128 v[124:127], v217 offset:50368
	ds_read_b128 v[230:233], v217 offset:58944
	ds_read_b128 v[234:237], v217 offset:59072
	ds_read_b128 v[238:241], v217 offset:50272
	ds_read_b128 v[242:245], v217 offset:50400
	s_waitcnt lgkmcnt(8)
	v_mfma_f32_32x32x16_bf16 v[84:99], v[80:83], v[168:171], v[84:99]
	ds_read_b128 v[80:83], v217 offset:58976
	ds_read_b128 v[246:249], v217 offset:59104
	s_waitcnt lgkmcnt(7)
	v_mfma_f32_32x32x16_bf16 v[100:115], v[120:123], v[164:167], v[100:115]
	v_add_f32_e32 v120, 0, v191
	v_add_f32_e32 v120, v193, v120
	v_add_f32_e32 v120, v189, v120
	v_add_f32_e32 v120, v192, v120
	v_add_f32_e32 v120, v188, v120
	v_add_f32_e32 v120, v190, v120
	v_add_f32_e32 v120, v186, v120
	s_waitcnt lgkmcnt(5)
	v_mfma_f32_32x32x16_bf16 v[84:99], v[230:233], v[164:167], v[84:99]
	v_add_f32_e32 v120, v187, v120
	v_add_f32_e32 v120, v179, v120
	v_add_f32_e32 v120, v184, v120
	v_exp_f32_e32 v122, v139
	v_exp_f32_e32 v123, v136
	v_exp_f32_e32 v136, v137
	s_waitcnt lgkmcnt(3)
	v_mfma_f32_32x32x16_bf16 v[100:115], v[238:241], v[148:151], v[100:115]
	s_waitcnt lgkmcnt(1)
	v_mfma_f32_32x32x16_bf16 v[84:99], v[80:83], v[148:151], v[84:99]
	v_add_f32_e32 v80, v177, v120
	v_add_f32_e32 v80, v182, v80
	v_add_f32_e32 v80, v176, v80
	v_add_f32_e32 v80, v185, v80
	v_add_f32_e32 v80, v178, v80
	v_add_f32_e32 v80, v183, v80
	v_add_f32_e32 v80, v142, v80
	v_mfma_f32_32x32x16_bf16 v[100:115], v[6:9], v[152:155], v[100:115]
	v_add_f32_e32 v6, v143, v80
	v_add_f32_e32 v6, v140, v6
	v_add_f32_e32 v6, v141, v6
	v_add_f32_e32 v6, v138, v6
	v_add_f32_e32 v6, v122, v6
	v_add_f32_e32 v6, v123, v6
	v_add_f32_e32 v6, v136, v6
	v_mfma_f32_32x32x16_bf16 v[84:99], v[10:13], v[152:155], v[84:99]
	v_add_f32_e32 v6, v134, v6
	v_add_f32_e32 v6, v135, v6
	v_add_f32_e32 v6, v132, v6
	v_add_f32_e32 v6, v133, v6
	v_add_f32_e32 v6, v130, v6
	v_add_f32_e32 v6, v131, v6
	v_add_f32_e32 v6, v128, v6
	v_mfma_f32_32x32x16_bf16 v[100:115], v[116:119], v[156:159], v[100:115]
	v_add_f32_e32 v199, v129, v6
	v_mov_b32_e32 v207, v199
	s_nop 1
	v_permlane32_swap_b32_e32 v199, v207
	v_cvt_pk_bf16_f32 v80, v191, v193
	v_cvt_pk_bf16_f32 v81, v189, v192
	v_cvt_pk_bf16_f32 v82, v188, v190
	v_mfma_f32_32x32x16_bf16 v[84:99], v[2:5], v[156:159], v[84:99]
	v_cvt_pk_bf16_f32 v83, v186, v187
	v_cvt_pk_bf16_f32 v116, v179, v184
	v_cvt_pk_bf16_f32 v117, v177, v182
	v_cvt_pk_bf16_f32 v118, v176, v185
	v_cvt_pk_bf16_f32 v119, v178, v183
	v_cvt_pk_bf16_f32 v120, v142, v143
	v_cvt_pk_bf16_f32 v121, v140, v141
	v_mfma_f32_32x32x16_bf16 v[100:115], v[124:127], v[160:163], v[100:115]
	v_cvt_pk_bf16_f32 v122, v138, v122
	v_cvt_pk_bf16_f32 v123, v123, v136
	v_cvt_pk_bf16_f32 v124, v134, v135
	v_cvt_pk_bf16_f32 v125, v132, v133
	v_cvt_pk_bf16_f32 v126, v130, v131
	v_cvt_pk_bf16_f32 v127, v128, v129
	v_permlane32_swap_b32_e32 v80, v82
	v_mfma_f32_32x32x16_bf16 v[84:99], v[234:237], v[160:163], v[84:99]
	v_permlane32_swap_b32_e32 v81, v83
	v_permlane32_swap_b32_e32 v116, v118
	v_permlane32_swap_b32_e32 v117, v119
	v_permlane32_swap_b32_e32 v120, v122
	v_mfma_f32_32x32x16_bf16 v[100:115], v[242:245], v[144:147], v[100:115]
	v_permlane32_swap_b32_e32 v121, v123
	v_permlane32_swap_b32_e32 v124, v126
	v_permlane32_swap_b32_e32 v125, v127
	s_waitcnt lgkmcnt(0)
	v_mfma_f32_32x32x16_bf16 v[84:99], v[246:249], v[144:147], v[84:99]
	v_add_u32_e32 v234, s60, v201
	v_add_u32_e32 v2, 1, v234
	v_add_u32_e32 v4, 33, v234
	v_ashrrev_i32_e32 v3, 31, v2
	v_ashrrev_i32_e32 v5, 31, v4
	v_lshlrev_b64 v[10:11], 8, v[2:3]
	v_lshlrev_b64 v[12:13], 8, v[4:5]
	v_lshl_add_u64 v[2:3], v[14:15], 0, v[10:11]
	v_lshl_add_u64 v[6:7], v[14:15], 0, v[12:13]
	v_lshl_add_u64 v[10:11], v[208:209], 0, v[10:11]
	global_load_dwordx4 v[2:5], v[2:3], off
	s_nop 0
	global_load_dwordx4 v[6:9], v[6:7], off
	v_lshl_add_u64 v[128:129], v[208:209], 0, v[12:13]
	global_load_dwordx4 v[10:13], v[10:11], off
	s_nop 0
	global_load_dwordx4 v[176:179], v[128:129], off
	ds_read_b64_tr_b16 v[128:129], v213 offset:0
	ds_read_b64_tr_b16 v[130:131], v213 offset:0x800
	ds_read_b64_tr_b16 v[132:133], v213 offset:0x1000
	ds_read_b64_tr_b16 v[134:135], v213 offset:0x1800
	ds_read_b64_tr_b16 v[136:137], v213 offset:0x2000
	ds_read_b64_tr_b16 v[138:139], v213 offset:0x2800
	ds_read_b64_tr_b16 v[140:141], v213 offset:0x3000
	ds_read_b64_tr_b16 v[142:143], v213 offset:0x3800
	s_nop 0
	s_waitcnt lgkmcnt(6)
	v_mfma_f32_32x32x16_bf16 v[64:79], v[80:83], v[128:131], v[64:79]
	ds_read_b64_tr_b16 v[128:129], v213 offset:0x200
	ds_read_b64_tr_b16 v[130:131], v213 offset:0xa00
	s_waitcnt lgkmcnt(6)
	v_mfma_f32_32x32x16_bf16 v[64:79], v[116:119], v[132:135], v[64:79]
	ds_read_b64_tr_b16 v[132:133], v213 offset:0x1200
	ds_read_b64_tr_b16 v[134:135], v213 offset:0x1a00
	s_waitcnt lgkmcnt(6)
	v_mfma_f32_32x32x16_bf16 v[64:79], v[120:123], v[136:139], v[64:79]
	ds_read_b64_tr_b16 v[136:137], v213 offset:0x2200
	ds_read_b64_tr_b16 v[138:139], v213 offset:0x2a00
	ds_read_b64_tr_b16 v[182:183], v213 offset:0x3200
	ds_read_b64_tr_b16 v[184:185], v213 offset:0x3a00
	s_waitcnt lgkmcnt(8)
	v_mfma_f32_32x32x16_bf16 v[64:79], v[124:127], v[140:143], v[64:79]
	s_waitcnt lgkmcnt(6)
	v_mfma_f32_32x32x16_bf16 v[48:63], v[80:83], v[128:131], v[48:63]
	ds_read_b64_tr_b16 v[128:129], v213 offset:0x400
	ds_read_b64_tr_b16 v[130:131], v213 offset:0xc00
	s_waitcnt lgkmcnt(6)
	v_mfma_f32_32x32x16_bf16 v[48:63], v[116:119], v[132:135], v[48:63]
	ds_read_b64_tr_b16 v[132:133], v213 offset:0x1400
	ds_read_b64_tr_b16 v[134:135], v213 offset:0x1c00
	s_waitcnt lgkmcnt(6)
	v_mfma_f32_32x32x16_bf16 v[48:63], v[120:123], v[136:139], v[48:63]
	ds_read_b64_tr_b16 v[136:137], v213 offset:0x2400
	ds_read_b64_tr_b16 v[138:139], v213 offset:0x2c00
	ds_read_b64_tr_b16 v[140:141], v213 offset:0x3400
	ds_read_b64_tr_b16 v[142:143], v213 offset:0x3c00
	s_waitcnt lgkmcnt(8)
	v_mfma_f32_32x32x16_bf16 v[48:63], v[124:127], v[182:185], v[48:63]
	s_waitcnt lgkmcnt(6)
	v_mfma_f32_32x32x16_bf16 v[32:47], v[80:83], v[128:131], v[32:47]
	ds_read_b64_tr_b16 v[128:129], v213 offset:0x600
	ds_read_b64_tr_b16 v[130:131], v213 offset:0xe00
	s_waitcnt lgkmcnt(6)
	v_mfma_f32_32x32x16_bf16 v[32:47], v[116:119], v[132:135], v[32:47]
	ds_read_b64_tr_b16 v[132:133], v213 offset:0x1600
	ds_read_b64_tr_b16 v[134:135], v213 offset:0x1e00
	s_waitcnt lgkmcnt(6)
	v_mfma_f32_32x32x16_bf16 v[32:47], v[120:123], v[136:139], v[32:47]
	ds_read_b64_tr_b16 v[136:137], v213 offset:0x2600
	ds_read_b64_tr_b16 v[138:139], v213 offset:0x2e00
	ds_read_b64_tr_b16 v[182:183], v213 offset:0x3600
	ds_read_b64_tr_b16 v[184:185], v213 offset:0x3e00
	s_waitcnt lgkmcnt(8)
	v_mfma_f32_32x32x16_bf16 v[32:47], v[124:127], v[140:143], v[32:47]
	s_waitcnt lgkmcnt(6)
	v_mfma_f32_32x32x16_bf16 v[16:31], v[80:83], v[128:131], v[16:31]
	s_cmp_le_i32 s60, s55
	s_cselect_b64 s[46:47], -1, 0
	s_cmp_gt_i32 s6, s56
	s_cselect_b64 s[6:7], -1, 0
	s_and_b64 s[6:7], s[46:47], s[6:7]
	s_and_b64 vcc, exec, s[6:7]
	s_waitcnt lgkmcnt(4)
	v_mfma_f32_32x32x16_bf16 v[16:31], v[116:119], v[132:135], v[16:31]
	s_waitcnt lgkmcnt(2)
	v_mfma_f32_32x32x16_bf16 v[16:31], v[120:123], v[136:139], v[16:31]
	s_waitcnt lgkmcnt(0)
	v_mfma_f32_32x32x16_bf16 v[16:31], v[124:127], v[182:185], v[16:31]
	s_cbranch_vccnz .LBB3_35
	v_add_u32_e32 v80, 0x7b, v0
	v_cmp_gt_u32_e32 vcc, s21, v80
	v_add_u32_e32 v80, 0x5b, v0
	s_nop 0
	v_cndmask_b32_e32 v100, v221, v100, vcc
	v_cmp_gt_u32_e32 vcc, s21, v80
	v_add_u32_e32 v80, 0x7a, v0
	s_nop 0
	v_cndmask_b32_e32 v84, v221, v84, vcc
	v_cmp_gt_u32_e32 vcc, s21, v80
	v_add_u32_e32 v80, 0x5a, v0
	s_nop 0
	v_cndmask_b32_e32 v101, v221, v101, vcc
	v_cmp_gt_u32_e32 vcc, s21, v80
	v_add_u32_e32 v80, 0x79, v0
	s_nop 0
	v_cndmask_b32_e32 v85, v221, v85, vcc
	v_cmp_gt_u32_e32 vcc, s21, v80
	v_add_u32_e32 v80, 0x59, v0
	s_nop 0
	v_cndmask_b32_e32 v102, v221, v102, vcc
	v_cmp_gt_u32_e32 vcc, s21, v80
	v_add_u32_e32 v80, 0x78, v0
	s_nop 0
	v_cndmask_b32_e32 v86, v221, v86, vcc
	v_cmp_gt_u32_e32 vcc, s21, v80
	v_add_u32_e32 v80, 0x58, v0
	s_nop 0
	v_cndmask_b32_e32 v103, v221, v103, vcc
	v_cmp_gt_u32_e32 vcc, s21, v80
	v_add_u32_e32 v80, 0x73, v0
	s_nop 0
	v_cndmask_b32_e32 v87, v221, v87, vcc
	v_cmp_gt_u32_e32 vcc, s21, v80
	v_add_u32_e32 v80, 0x53, v0
	s_nop 0
	v_cndmask_b32_e32 v104, v221, v104, vcc
	v_cmp_gt_u32_e32 vcc, s21, v80
	v_add_u32_e32 v80, 0x72, v0
	s_nop 0
	v_cndmask_b32_e32 v88, v221, v88, vcc
	v_cmp_gt_u32_e32 vcc, s21, v80
	v_add_u32_e32 v80, 0x52, v0
	s_nop 0
	v_cndmask_b32_e32 v105, v221, v105, vcc
	v_cmp_gt_u32_e32 vcc, s21, v80
	v_add_u32_e32 v80, 0x71, v0
	s_nop 0
	v_cndmask_b32_e32 v89, v221, v89, vcc
	v_cmp_gt_u32_e32 vcc, s21, v80
	v_add_u32_e32 v80, 0x51, v0
	s_nop 0
	v_cndmask_b32_e32 v106, v221, v106, vcc
	v_cmp_gt_u32_e32 vcc, s21, v80
	v_add_u32_e32 v80, 0x70, v0
	s_nop 0
	v_cndmask_b32_e32 v90, v221, v90, vcc
	v_cmp_gt_u32_e32 vcc, s21, v80
	v_add_u32_e32 v80, 0x50, v0
	s_nop 0
	v_cndmask_b32_e32 v107, v221, v107, vcc
	v_cmp_gt_u32_e32 vcc, s21, v80
	v_add_u32_e32 v80, 0x6b, v0
	s_nop 0
	v_cndmask_b32_e32 v91, v221, v91, vcc
	v_cmp_gt_u32_e32 vcc, s21, v80
	v_add_u32_e32 v80, 0x4b, v0
	s_nop 0
	v_cndmask_b32_e32 v108, v221, v108, vcc
	v_cmp_gt_u32_e32 vcc, s21, v80
	v_add_u32_e32 v80, 0x6a, v0
	s_nop 0
	v_cndmask_b32_e32 v92, v221, v92, vcc
	v_cmp_gt_u32_e32 vcc, s21, v80
	v_add_u32_e32 v80, 0x4a, v0
	s_nop 0
	v_cndmask_b32_e32 v109, v221, v109, vcc
	v_cmp_gt_u32_e32 vcc, s21, v80
	v_add_u32_e32 v80, 0x69, v0
	s_nop 0
	v_cndmask_b32_e32 v93, v221, v93, vcc
	v_cmp_gt_u32_e32 vcc, s21, v80
	v_add_u32_e32 v80, 0x49, v0
	s_nop 0
	v_cndmask_b32_e32 v110, v221, v110, vcc
	v_cmp_gt_u32_e32 vcc, s21, v80
	v_add_u32_e32 v80, 0x68, v0
	s_nop 0
	v_cndmask_b32_e32 v94, v221, v94, vcc
	v_cmp_gt_u32_e32 vcc, s21, v80
	v_add_u32_e32 v80, 0x48, v0
	s_nop 0
	v_cndmask_b32_e32 v111, v221, v111, vcc
	v_cmp_gt_u32_e32 vcc, s21, v80
	v_add_u32_e32 v80, 0x63, v0
	s_nop 0
	v_cndmask_b32_e32 v95, v221, v95, vcc
	v_cmp_gt_u32_e32 vcc, s21, v80
	v_add_u32_e32 v80, 0x43, v0
	s_nop 0
	v_cndmask_b32_e32 v112, v221, v112, vcc
	v_cmp_gt_u32_e32 vcc, s21, v80
	v_add_u32_e32 v80, 0x62, v0
	s_nop 0
	v_cndmask_b32_e32 v96, v221, v96, vcc
	v_cmp_gt_u32_e32 vcc, s21, v80
	v_add_u32_e32 v80, 0x42, v0
	s_nop 0
	v_cndmask_b32_e32 v113, v221, v113, vcc
	v_cmp_gt_u32_e32 vcc, s21, v80
	v_add_u32_e32 v80, 0x61, v0
	s_nop 0
	v_cndmask_b32_e32 v97, v221, v97, vcc
	v_cmp_gt_u32_e32 vcc, s21, v80
	v_add_u32_e32 v80, 0x41, v0
	s_nop 0
	v_cndmask_b32_e32 v114, v221, v114, vcc
	v_cmp_gt_u32_e32 vcc, s21, v80
	v_add_u32_e32 v80, 0x60, v0
	s_nop 0
	v_cndmask_b32_e32 v98, v221, v98, vcc
	v_cmp_gt_u32_e32 vcc, s21, v80
	v_add_u32_e32 v80, 64, v0
	s_nop 0
	v_cndmask_b32_e32 v115, v221, v115, vcc
	v_cmp_gt_u32_e32 vcc, s21, v80
	s_nop 1
	v_cndmask_b32_e32 v99, v221, v99, vcc
.LBB3_35:
	v_max_f32_e32 v80, v101, v101
	v_max_f32_e32 v81, v100, v100
	v_max_f32_e32 v80, v81, v80
	v_max3_f32 v80, v80, v102, v103
	v_max3_f32 v80, v80, v104, v105
	v_max3_f32 v80, v80, v106, v107
	v_max3_f32 v80, v80, v108, v109
	v_max3_f32 v80, v80, v110, v111
	v_max3_f32 v80, v80, v112, v113
	v_max3_f32 v80, v80, v114, v115
	v_max3_f32 v80, v80, v84, v85
	v_max3_f32 v80, v80, v86, v87
	v_max3_f32 v80, v80, v88, v89
	v_max3_f32 v80, v80, v90, v91
	v_max3_f32 v80, v80, v92, v93
	v_max3_f32 v80, v80, v94, v95
	v_max3_f32 v80, v80, v96, v97
	v_max3_f32 v80, v80, v98, v99
	v_mov_b32_e32 v81, v80
	s_nop 1
	v_permlane32_swap_b32_e32 v80, v81
	v_max_f32_e32 v81, v81, v81
	v_max_f32_e32 v80, v80, v80
	v_max_f32_e32 v80, v80, v81
	v_max_f32_e32 v82, v180, v180
	v_sub_f32_e32 v81, v80, v180
	v_max_f32_e32 v80, v82, v80
	v_sub_f32_e32 v82, v180, v80
	v_mul_f32_e32 v82, 0x3e0293ee, v82
	v_mul_f32_e32 v81, 0x3db504f3, v81
	v_exp_f32_e32 v82, v82
	v_cmp_ge_f32_e32 vcc, s20, v81
	s_cmp_eq_u64 vcc, exec
	s_cselect_b64 s[6:7], -1, 0
	s_barrier
	s_waitcnt vmcnt(0)
	v_cndmask_b32_e64 v230, v82, 1.0, s[6:7]
	v_cmp_gt_f32_e32 vcc, 1.0, v230
	s_waitcnt vmcnt(3)
	ds_write_b128 v215, v[2:5]
	s_waitcnt vmcnt(2)
	ds_write_b128 v216, v[6:9]
	s_waitcnt vmcnt(1)
	ds_write_b128 v222, v[10:13] offset:32768
	s_waitcnt vmcnt(0)
	ds_write_b128 v222, v[176:179] offset:41472
	s_cbranch_vccz .LBB3_39
	s_and_saveexec_b64 s[46:47], s[0:1]
	ds_write_b32 v226, v230 offset:128
	s_or_b64 exec, exec, s[46:47]
	s_waitcnt lgkmcnt(0)
	ds_read_b128 v[116:119], v225 offset:224
	ds_read_b128 v[120:123], v225 offset:192
	ds_read_b128 v[124:127], v225 offset:160
	ds_read_b128 v[128:131], v225 offset:128
	s_waitcnt lgkmcnt(3)
	v_pk_mul_f32 v[78:79], v[78:79], v[118:119]
	s_waitcnt lgkmcnt(2)
	v_pk_mul_f32 v[74:75], v[74:75], v[122:123]
	s_waitcnt lgkmcnt(1)
	v_pk_mul_f32 v[70:71], v[70:71], v[126:127]
	s_waitcnt lgkmcnt(0)
	v_pk_mul_f32 v[66:67], v[66:67], v[130:131]
	v_pk_mul_f32 v[76:77], v[76:77], v[116:117]
	v_pk_mul_f32 v[72:73], v[72:73], v[120:121]
	v_pk_mul_f32 v[68:69], v[68:69], v[124:125]
	v_pk_mul_f32 v[64:65], v[64:65], v[128:129]
	v_pk_mul_f32 v[62:63], v[62:63], v[118:119]
	v_pk_mul_f32 v[58:59], v[58:59], v[122:123]
	v_pk_mul_f32 v[54:55], v[54:55], v[126:127]
	v_pk_mul_f32 v[50:51], v[50:51], v[130:131]
	v_pk_mul_f32 v[60:61], v[60:61], v[116:117]
	v_pk_mul_f32 v[56:57], v[56:57], v[120:121]
	v_pk_mul_f32 v[52:53], v[52:53], v[124:125]
	v_pk_mul_f32 v[48:49], v[48:49], v[128:129]
	v_pk_mul_f32 v[46:47], v[46:47], v[118:119]
	v_pk_mul_f32 v[42:43], v[42:43], v[122:123]
	v_pk_mul_f32 v[38:39], v[38:39], v[126:127]
	v_pk_mul_f32 v[34:35], v[34:35], v[130:131]
	v_pk_mul_f32 v[44:45], v[44:45], v[116:117]
	v_pk_mul_f32 v[40:41], v[40:41], v[120:121]
	v_pk_mul_f32 v[36:37], v[36:37], v[124:125]
	v_pk_mul_f32 v[32:33], v[32:33], v[128:129]
	v_pk_mul_f32 v[30:31], v[30:31], v[118:119]
	v_pk_mul_f32 v[26:27], v[26:27], v[122:123]
	v_pk_mul_f32 v[22:23], v[22:23], v[126:127]
	v_pk_mul_f32 v[18:19], v[18:19], v[130:131]
	v_pk_mul_f32 v[28:29], v[28:29], v[116:117]
	v_pk_mul_f32 v[24:25], v[24:25], v[120:121]
	v_pk_mul_f32 v[20:21], v[20:21], v[124:125]
	v_pk_mul_f32 v[16:17], v[16:17], v[128:129]
.LBB3_39:
	v_cndmask_b32_e64 v231, v80, v180, s[6:7]
	v_mul_f32_e32 v180, 0xbe0293ee, v231
	v_fmamk_f32 v80, v100, 0x3e0293ee, v180
	v_fmamk_f32 v81, v101, 0x3e0293ee, v180
	v_fmamk_f32 v82, v102, 0x3e0293ee, v180
	v_fmamk_f32 v83, v103, 0x3e0293ee, v180
	v_fmamk_f32 v116, v104, 0x3e0293ee, v180
	v_fmamk_f32 v117, v105, 0x3e0293ee, v180
	v_fmamk_f32 v118, v106, 0x3e0293ee, v180
	v_fmamk_f32 v119, v107, 0x3e0293ee, v180
	v_fmamk_f32 v120, v108, 0x3e0293ee, v180
	v_fmamk_f32 v121, v109, 0x3e0293ee, v180
	v_fmamk_f32 v122, v110, 0x3e0293ee, v180
	v_fmamk_f32 v123, v111, 0x3e0293ee, v180
	v_fmamk_f32 v112, v112, 0x3e0293ee, v180
	v_fmamk_f32 v113, v113, 0x3e0293ee, v180
	v_fmamk_f32 v114, v114, 0x3e0293ee, v180
	v_fmamk_f32 v115, v115, 0x3e0293ee, v180
	v_fmamk_f32 v100, v84, 0x3e0293ee, v180
	v_fmamk_f32 v109, v85, 0x3e0293ee, v180
	v_fmamk_f32 v110, v86, 0x3e0293ee, v180
	v_fmamk_f32 v111, v87, 0x3e0293ee, v180
	v_fmamk_f32 v181, v88, 0x3e0293ee, v180
	v_fmamk_f32 v101, v89, 0x3e0293ee, v180
	v_fmamk_f32 v102, v90, 0x3e0293ee, v180
	v_fmamk_f32 v103, v91, 0x3e0293ee, v180
	v_fmamk_f32 v104, v92, 0x3e0293ee, v180
	v_fmamk_f32 v105, v93, 0x3e0293ee, v180
	v_fmamk_f32 v106, v94, 0x3e0293ee, v180
	v_fmamk_f32 v107, v95, 0x3e0293ee, v180
	v_exp_f32_e32 v80, v80
	v_exp_f32_e32 v81, v81
	v_exp_f32_e32 v82, v82
	v_exp_f32_e32 v83, v83
	v_exp_f32_e32 v84, v116
	v_exp_f32_e32 v85, v117
	v_exp_f32_e32 v86, v118
	v_exp_f32_e32 v87, v119
	v_exp_f32_e32 v88, v120
	v_exp_f32_e32 v89, v121
	v_exp_f32_e32 v90, v122
	v_exp_f32_e32 v91, v123
	v_exp_f32_e32 v92, v112
	v_exp_f32_e32 v93, v113
	v_exp_f32_e32 v94, v114
	v_exp_f32_e32 v95, v115
	v_fmamk_f32 v108, v96, 0x3e0293ee, v180
	v_fmamk_f32 v182, v97, 0x3e0293ee, v180
	v_fmamk_f32 v183, v98, 0x3e0293ee, v180
	v_fmac_f32_e32 v180, 0x3e0293ee, v99
	s_waitcnt lgkmcnt(0)
	s_barrier
	ds_read_b128 v[96:99], v217 offset:32768
	ds_read_b128 v[112:115], v217 offset:41472
	v_exp_f32_e32 v101, v101
	v_exp_f32_e32 v102, v102
	v_exp_f32_e32 v103, v103
	s_waitcnt lgkmcnt(1)
	v_mfma_f32_32x32x16_bf16 v[128:143], v[96:99], v[172:175], 0
	ds_read_b128 v[96:99], v217 offset:32800
	ds_read_b128 v[184:187], v217 offset:41504
	v_exp_f32_e32 v104, v104
	v_exp_f32_e32 v105, v105
	v_exp_f32_e32 v106, v106
	v_exp_f32_e32 v107, v107
	v_exp_f32_e32 v108, v108
	s_waitcnt lgkmcnt(2)
	v_mfma_f32_32x32x16_bf16 v[112:127], v[112:115], v[172:175], 0
	s_waitcnt lgkmcnt(1)
	v_mfma_f32_32x32x16_bf16 v[128:143], v[96:99], v[168:171], v[128:143]
	s_waitcnt lgkmcnt(0)
	v_mfma_f32_32x32x16_bf16 v[112:127], v[184:187], v[168:171], v[112:127]
	ds_read_b128 v[96:99], v217 offset:32832
	ds_read_b128 v[184:187], v217 offset:41536
	s_waitcnt lgkmcnt(1)
	v_mfma_f32_32x32x16_bf16 v[128:143], v[96:99], v[164:167], v[128:143]
	s_waitcnt lgkmcnt(0)
	v_mfma_f32_32x32x16_bf16 v[112:127], v[184:187], v[164:167], v[112:127]
	ds_read_b128 v[96:99], v217 offset:32864
	ds_read_b128 v[184:187], v217 offset:41568
	s_waitcnt lgkmcnt(1)
	v_mfma_f32_32x32x16_bf16 v[128:143], v[96:99], v[148:151], v[128:143]
	s_waitcnt lgkmcnt(0)
	v_mfma_f32_32x32x16_bf16 v[112:127], v[184:187], v[148:151], v[112:127]
	ds_read_b128 v[96:99], v217 offset:32896
	ds_read_b128 v[184:187], v217 offset:41600
	s_waitcnt lgkmcnt(1)
	v_mfma_f32_32x32x16_bf16 v[128:143], v[96:99], v[152:155], v[128:143]
	s_waitcnt lgkmcnt(0)
	v_mfma_f32_32x32x16_bf16 v[112:127], v[184:187], v[152:155], v[112:127]
	ds_read_b128 v[96:99], v217 offset:32928
	ds_read_b128 v[184:187], v217 offset:41632
	s_waitcnt lgkmcnt(1)
	v_mfma_f32_32x32x16_bf16 v[128:143], v[96:99], v[156:159], v[128:143]
	s_waitcnt lgkmcnt(0)
	v_mfma_f32_32x32x16_bf16 v[112:127], v[184:187], v[156:159], v[112:127]
	ds_read_b128 v[96:99], v217 offset:32960
	ds_read_b128 v[184:187], v217 offset:41664
	s_waitcnt lgkmcnt(1)
	v_mfma_f32_32x32x16_bf16 v[128:143], v[96:99], v[160:163], v[128:143]
	s_waitcnt lgkmcnt(0)
	v_mfma_f32_32x32x16_bf16 v[112:127], v[184:187], v[160:163], v[112:127]
	ds_read_b128 v[96:99], v217 offset:32992
	ds_read_b128 v[184:187], v217 offset:41696
	s_waitcnt lgkmcnt(1)
	v_mfma_f32_32x32x16_bf16 v[128:143], v[96:99], v[144:147], v[128:143]
	v_exp_f32_e32 v99, v111
	v_exp_f32_e32 v111, v180
	v_add_f32_e32 v180, 0, v80
	v_add_f32_e32 v180, v81, v180
	v_add_f32_e32 v180, v82, v180
	v_add_f32_e32 v180, v83, v180
	v_add_f32_e32 v180, v84, v180
	v_add_f32_e32 v180, v85, v180
	v_add_f32_e32 v180, v86, v180
	v_add_f32_e32 v180, v87, v180
	v_add_f32_e32 v180, v88, v180
	v_add_f32_e32 v180, v89, v180
	v_add_f32_e32 v180, v90, v180
	v_add_f32_e32 v180, v91, v180
	v_exp_f32_e32 v96, v100
	v_add_f32_e32 v180, v92, v180
	v_exp_f32_e32 v97, v109
	v_add_f32_e32 v180, v93, v180
	v_exp_f32_e32 v98, v110
	v_add_f32_e32 v180, v94, v180
	v_add_f32_e32 v180, v95, v180
	v_exp_f32_e32 v100, v181
	v_add_f32_e32 v180, v96, v180
	v_add_f32_e32 v180, v97, v180
	v_add_f32_e32 v180, v98, v180
	v_add_f32_e32 v180, v99, v180
	v_add_f32_e32 v180, v100, v180
	v_add_f32_e32 v180, v101, v180
	v_add_f32_e32 v180, v102, v180
	v_add_f32_e32 v180, v103, v180
	v_add_f32_e32 v180, v104, v180
	v_exp_f32_e32 v109, v182
	v_add_f32_e32 v180, v105, v180
	s_waitcnt lgkmcnt(0)
	v_mfma_f32_32x32x16_bf16 v[112:127], v[184:187], v[144:147], v[112:127]
	v_exp_f32_e32 v110, v183
	v_add_f32_e32 v180, v106, v180
	v_add_f32_e32 v180, v107, v180
	v_add_f32_e32 v180, v108, v180
	v_add_f32_e32 v180, v109, v180
	v_add_f32_e32 v180, v110, v180
	v_add_f32_e32 v232, v111, v180
	v_mov_b32_e32 v233, v232
	v_cvt_pk_bf16_f32 v180, v80, v81
	v_cvt_pk_bf16_f32 v181, v82, v83
	v_cvt_pk_bf16_f32 v182, v84, v85
	v_cvt_pk_bf16_f32 v183, v86, v87
	v_cvt_pk_bf16_f32 v184, v88, v89
	v_cvt_pk_bf16_f32 v185, v90, v91
	v_cvt_pk_bf16_f32 v186, v92, v93
	v_cvt_pk_bf16_f32 v187, v94, v95
	v_cvt_pk_bf16_f32 v188, v96, v97
	v_cvt_pk_bf16_f32 v189, v98, v99
	v_cvt_pk_bf16_f32 v190, v100, v101
	v_cvt_pk_bf16_f32 v191, v102, v103
	v_cvt_pk_bf16_f32 v192, v104, v105
	v_cvt_pk_bf16_f32 v193, v106, v107
	v_cvt_pk_bf16_f32 v194, v108, v109
	v_cvt_pk_bf16_f32 v195, v110, v111
	s_nop 1
	v_permlane32_swap_b32_e32 v232, v233
	v_permlane32_swap_b32_e32 v180, v182
	v_permlane32_swap_b32_e32 v181, v183
	v_permlane32_swap_b32_e32 v184, v186
	v_permlane32_swap_b32_e32 v185, v187
	v_permlane32_swap_b32_e32 v188, v190
	v_permlane32_swap_b32_e32 v189, v191
	v_permlane32_swap_b32_e32 v192, v194
	v_permlane32_swap_b32_e32 v193, v195
	s_add_i32 s6, s59, 1
	s_cmp_lt_i32 s6, s58
	s_cselect_b64 s[46:47], -1, 0
	s_cmp_ge_i32 s6, s58
	s_cbranch_scc1 .LBB3_41
	v_add_u32_e32 v2, 0x41, v234
	v_add_u32_e32 v4, 0x61, v234
	v_ashrrev_i32_e32 v3, 31, v2
	v_ashrrev_i32_e32 v5, 31, v4
	v_lshlrev_b64 v[10:11], 8, v[2:3]
	v_lshlrev_b64 v[12:13], 8, v[4:5]
	v_lshl_add_u64 v[2:3], v[14:15], 0, v[10:11]
	v_lshl_add_u64 v[6:7], v[14:15], 0, v[12:13]
	v_lshl_add_u64 v[10:11], v[208:209], 0, v[10:11]
	v_lshl_add_u64 v[176:177], v[208:209], 0, v[12:13]
	global_load_dwordx4 v[2:5], v[2:3], off
	s_nop 0
	global_load_dwordx4 v[6:9], v[6:7], off
	s_nop 0
	global_load_dwordx4 v[10:13], v[10:11], off
	s_nop 0
	global_load_dwordx4 v[176:179], v[176:177], off
.LBB3_41:
	ds_read_b64_tr_b16 v[234:235], v213 offset:0x4000
	ds_read_b64_tr_b16 v[236:237], v213 offset:0x4800
	ds_read_b64_tr_b16 v[238:239], v213 offset:0x5000
	ds_read_b64_tr_b16 v[240:241], v213 offset:0x5800
	ds_read_b64_tr_b16 v[242:243], v213 offset:0x6000
	ds_read_b64_tr_b16 v[244:245], v213 offset:0x6800
	ds_read_b64_tr_b16 v[246:247], v213 offset:0x7000
	ds_read_b64_tr_b16 v[248:249], v213 offset:0x7800
	s_add_i32 s6, s60, 64
	s_add_i32 s61, s60, 1
	s_waitcnt lgkmcnt(6)
	v_mfma_f32_32x32x16_bf16 v[64:79], v[180:183], v[234:237], v[64:79]
	ds_read_b64_tr_b16 v[234:235], v213 offset:0x4200
	ds_read_b64_tr_b16 v[236:237], v213 offset:0x4a00
	s_waitcnt lgkmcnt(6)
	v_mfma_f32_32x32x16_bf16 v[64:79], v[184:187], v[238:241], v[64:79]
	ds_read_b64_tr_b16 v[238:239], v213 offset:0x5200
	ds_read_b64_tr_b16 v[240:241], v213 offset:0x5a00
	s_waitcnt lgkmcnt(6)
	v_mfma_f32_32x32x16_bf16 v[64:79], v[188:191], v[242:245], v[64:79]
	ds_read_b64_tr_b16 v[242:243], v213 offset:0x6200
	ds_read_b64_tr_b16 v[244:245], v213 offset:0x6a00
	ds_read_b64_tr_b16 v[250:251], v213 offset:0x7200
	ds_read_b64_tr_b16 v[252:253], v213 offset:0x7a00
	s_waitcnt lgkmcnt(8)
	v_mfma_f32_32x32x16_bf16 v[64:79], v[192:195], v[246:249], v[64:79]
	s_waitcnt lgkmcnt(6)
	v_mfma_f32_32x32x16_bf16 v[48:63], v[180:183], v[234:237], v[48:63]
	ds_read_b64_tr_b16 v[234:235], v213 offset:0x4400
	ds_read_b64_tr_b16 v[236:237], v213 offset:0x4c00
	s_waitcnt lgkmcnt(6)
	v_mfma_f32_32x32x16_bf16 v[48:63], v[184:187], v[238:241], v[48:63]
	ds_read_b64_tr_b16 v[238:239], v213 offset:0x5400
	ds_read_b64_tr_b16 v[240:241], v213 offset:0x5c00
	s_waitcnt lgkmcnt(6)
	v_mfma_f32_32x32x16_bf16 v[48:63], v[188:191], v[242:245], v[48:63]
	ds_read_b64_tr_b16 v[242:243], v213 offset:0x6400
	ds_read_b64_tr_b16 v[244:245], v213 offset:0x6c00
	ds_read_b64_tr_b16 v[246:247], v213 offset:0x7400
	ds_read_b64_tr_b16 v[248:249], v213 offset:0x7c00
	s_waitcnt lgkmcnt(8)
	v_mfma_f32_32x32x16_bf16 v[48:63], v[192:195], v[250:253], v[48:63]
	s_waitcnt lgkmcnt(6)
	v_mfma_f32_32x32x16_bf16 v[32:47], v[180:183], v[234:237], v[32:47]
	ds_read_b64_tr_b16 v[234:235], v213 offset:0x4600
	ds_read_b64_tr_b16 v[236:237], v213 offset:0x4e00
	s_waitcnt lgkmcnt(6)
	v_mfma_f32_32x32x16_bf16 v[32:47], v[184:187], v[238:241], v[32:47]
	ds_read_b64_tr_b16 v[238:239], v213 offset:0x5600
	ds_read_b64_tr_b16 v[240:241], v213 offset:0x5e00
	s_waitcnt lgkmcnt(6)
	v_mfma_f32_32x32x16_bf16 v[32:47], v[188:191], v[242:245], v[32:47]
	ds_read_b64_tr_b16 v[242:243], v213 offset:0x6600
	ds_read_b64_tr_b16 v[244:245], v213 offset:0x6e00
	ds_read_b64_tr_b16 v[250:251], v213 offset:0x7600
	ds_read_b64_tr_b16 v[252:253], v213 offset:0x7e00
	s_waitcnt lgkmcnt(8)
	v_mfma_f32_32x32x16_bf16 v[32:47], v[192:195], v[246:249], v[32:47]
	s_waitcnt lgkmcnt(6)
	v_mfma_f32_32x32x16_bf16 v[16:31], v[180:183], v[234:237], v[16:31]
	s_cmp_le_i32 s6, s55
	s_cselect_b64 s[6:7], -1, 0
	s_cmp_gt_i32 s61, s56
	s_cselect_b64 s[62:63], -1, 0
	s_and_b64 s[6:7], s[6:7], s[62:63]
	s_and_b64 vcc, exec, s[6:7]
	s_waitcnt lgkmcnt(4)
	v_mfma_f32_32x32x16_bf16 v[16:31], v[184:187], v[238:241], v[16:31]
	s_waitcnt lgkmcnt(2)
	v_mfma_f32_32x32x16_bf16 v[16:31], v[188:191], v[242:245], v[16:31]
	s_waitcnt lgkmcnt(0)
	v_mfma_f32_32x32x16_bf16 v[16:31], v[192:195], v[250:253], v[16:31]
	s_cbranch_vccnz .LBB3_43
	v_add_u32_e32 v180, 59, v0
	v_cmp_gt_u32_e32 vcc, s21, v180
	v_add_u32_e32 v180, 27, v0
	s_nop 0
	v_cndmask_b32_e32 v128, v221, v128, vcc
	v_cmp_gt_u32_e32 vcc, s21, v180
	v_add_u32_e32 v180, 58, v0
	s_nop 0
	v_cndmask_b32_e32 v112, v221, v112, vcc
	v_cmp_gt_u32_e32 vcc, s21, v180
	v_add_u32_e32 v180, 26, v0
	s_nop 0
	v_cndmask_b32_e32 v129, v221, v129, vcc
	v_cmp_gt_u32_e32 vcc, s21, v180
	v_add_u32_e32 v180, 57, v0
	s_nop 0
	v_cndmask_b32_e32 v113, v221, v113, vcc
	v_cmp_gt_u32_e32 vcc, s21, v180
	v_add_u32_e32 v180, 25, v0
	s_nop 0
	v_cndmask_b32_e32 v130, v221, v130, vcc
	v_cmp_gt_u32_e32 vcc, s21, v180
	v_add_u32_e32 v180, 56, v0
	s_nop 0
	v_cndmask_b32_e32 v114, v221, v114, vcc
	v_cmp_gt_u32_e32 vcc, s21, v180
	v_add_u32_e32 v180, 24, v0
	s_nop 0
	v_cndmask_b32_e32 v131, v221, v131, vcc
	v_cmp_gt_u32_e32 vcc, s21, v180
	v_add_u32_e32 v180, 51, v0
	s_nop 0
	v_cndmask_b32_e32 v115, v221, v115, vcc
	v_cmp_gt_u32_e32 vcc, s21, v180
	v_add_u32_e32 v180, 19, v0
	s_nop 0
	v_cndmask_b32_e32 v132, v221, v132, vcc
	v_cmp_gt_u32_e32 vcc, s21, v180
	v_add_u32_e32 v180, 50, v0
	s_nop 0
	v_cndmask_b32_e32 v116, v221, v116, vcc
	v_cmp_gt_u32_e32 vcc, s21, v180
	v_add_u32_e32 v180, 18, v0
	s_nop 0
	v_cndmask_b32_e32 v133, v221, v133, vcc
	v_cmp_gt_u32_e32 vcc, s21, v180
	v_add_u32_e32 v180, 49, v0
	s_nop 0
	v_cndmask_b32_e32 v117, v221, v117, vcc
	v_cmp_gt_u32_e32 vcc, s21, v180
	v_add_u32_e32 v180, 17, v0
	s_nop 0
	v_cndmask_b32_e32 v134, v221, v134, vcc
	v_cmp_gt_u32_e32 vcc, s21, v180
	v_add_u32_e32 v180, 48, v0
	s_nop 0
	v_cndmask_b32_e32 v118, v221, v118, vcc
	v_cmp_gt_u32_e32 vcc, s21, v180
	v_add_u32_e32 v180, 16, v0
	s_nop 0
	v_cndmask_b32_e32 v135, v221, v135, vcc
	v_cmp_gt_u32_e32 vcc, s21, v180
	v_add_u32_e32 v180, 43, v0
	s_nop 0
	v_cndmask_b32_e32 v119, v221, v119, vcc
	v_cmp_gt_u32_e32 vcc, s21, v180
	v_add_u32_e32 v180, 11, v0
	s_nop 0
	v_cndmask_b32_e32 v136, v221, v136, vcc
	v_cmp_gt_u32_e32 vcc, s21, v180
	v_add_u32_e32 v180, 42, v0
	s_nop 0
	v_cndmask_b32_e32 v120, v221, v120, vcc
	v_cmp_gt_u32_e32 vcc, s21, v180
	v_add_u32_e32 v180, 10, v0
	s_nop 0
	v_cndmask_b32_e32 v137, v221, v137, vcc
	v_cmp_gt_u32_e32 vcc, s21, v180
	v_add_u32_e32 v180, 41, v0
	s_nop 0
	v_cndmask_b32_e32 v121, v221, v121, vcc
	v_cmp_gt_u32_e32 vcc, s21, v180
	v_add_u32_e32 v180, 9, v0
	s_nop 0
	v_cndmask_b32_e32 v138, v221, v138, vcc
	v_cmp_gt_u32_e32 vcc, s21, v180
	v_add_u32_e32 v180, 40, v0
	s_nop 0
	v_cndmask_b32_e32 v122, v221, v122, vcc
	v_cmp_gt_u32_e32 vcc, s21, v180
	v_add_u32_e32 v180, 8, v0
	s_nop 0
	v_cndmask_b32_e32 v139, v221, v139, vcc
	v_cmp_gt_u32_e32 vcc, s21, v180
	v_add_u32_e32 v180, 35, v0
	s_nop 0
	v_cndmask_b32_e32 v123, v221, v123, vcc
	v_cmp_gt_u32_e32 vcc, s21, v180
	v_add_u32_e32 v180, 3, v0
	s_nop 0
	v_cndmask_b32_e32 v140, v221, v140, vcc
	v_cmp_gt_u32_e32 vcc, s21, v180
	v_add_u32_e32 v180, 34, v0
	s_nop 0
	v_cndmask_b32_e32 v124, v221, v124, vcc
	v_cmp_gt_u32_e32 vcc, s21, v180
	v_add_u32_e32 v180, 2, v0
	s_nop 0
	v_cndmask_b32_e32 v141, v221, v141, vcc
	v_cmp_gt_u32_e32 vcc, s21, v180
	v_add_u32_e32 v180, 33, v0
	s_nop 0
	v_cndmask_b32_e32 v125, v221, v125, vcc
	v_cmp_gt_u32_e32 vcc, s21, v180
	v_add_u32_e32 v180, 1, v0
	s_nop 0
	v_cndmask_b32_e32 v142, v221, v142, vcc
	v_cmp_gt_u32_e32 vcc, s21, v180
	v_add_u32_e32 v180, 32, v0
	s_nop 0
	v_cndmask_b32_e32 v126, v221, v126, vcc
	v_cmp_gt_u32_e32 vcc, s21, v180
	s_nop 1
	v_cndmask_b32_e32 v143, v221, v143, vcc
	v_cmp_gt_u32_e32 vcc, s21, v0
	s_nop 1
	v_cndmask_b32_e32 v127, v221, v127, vcc
.LBB3_43:
	v_max_f32_e32 v180, v129, v129
	v_max_f32_e32 v181, v128, v128
	v_max_f32_e32 v180, v181, v180
	v_max3_f32 v180, v180, v130, v131
	v_max3_f32 v180, v180, v132, v133
	v_max3_f32 v180, v180, v134, v135
	v_max3_f32 v180, v180, v136, v137
	v_max3_f32 v180, v180, v138, v139
	v_max3_f32 v180, v180, v140, v141
	v_max3_f32 v180, v180, v142, v143
	v_max3_f32 v180, v180, v112, v113
	v_max3_f32 v180, v180, v114, v115
	v_max3_f32 v180, v180, v116, v117
	v_max3_f32 v180, v180, v118, v119
	v_max3_f32 v180, v180, v120, v121
	v_max3_f32 v180, v180, v122, v123
	v_max3_f32 v180, v180, v124, v125
	v_max3_f32 v180, v180, v126, v127
	v_mov_b32_e32 v181, v180
	s_nop 1
	v_permlane32_swap_b32_e32 v180, v181
	v_max_f32_e32 v181, v181, v181
	v_max_f32_e32 v180, v180, v180
	v_max_f32_e32 v180, v180, v181
	v_sub_f32_e32 v181, v180, v231
	v_mul_f32_e32 v181, 0x3db504f3, v181
	v_cmp_ge_f32_e32 vcc, s20, v181
	s_cmp_eq_u64 vcc, exec
	s_cselect_b64 s[6:7], -1, 0
	s_andn2_b64 vcc, exec, s[46:47]
	s_barrier
	s_cbranch_vccnz .LBB3_45
	s_waitcnt vmcnt(0)
	s_waitcnt vmcnt(3)
	ds_write_b128 v215, v[2:5] offset:16384
	s_waitcnt vmcnt(2)
	ds_write_b128 v216, v[6:9] offset:16384
	s_waitcnt vmcnt(1)
	ds_write_b128 v222, v[10:13] offset:50176
	s_waitcnt vmcnt(0)
	ds_write_b128 v222, v[176:179] offset:58880

.LBB3_49:
	s_bitcmp0_b32 s58, 0
	s_cselect_b64 s[6:7], -1, 0
	s_and_b64 vcc, exec, s[6:7]
	s_cbranch_vccz .LBB3_51
	ds_read_b128 v[2:5], v217 offset:50176
	ds_read_b128 v[6:9], v217 offset:50304
	s_waitcnt lgkmcnt(1)
	v_mfma_f32_32x32x16_bf16 v[80:95], v[2:5], v[172:175], 0
	ds_read_b128 v[2:5], v217 offset:58880
	ds_read_b128 v[10:13], v217 offset:59008
	s_waitcnt lgkmcnt(1)
	v_mfma_f32_32x32x16_bf16 v[96:111], v[2:5], v[172:175], 0
	ds_read_b128 v[2:5], v217 offset:50208
	s_waitcnt vmcnt(1)
	ds_read_b128 v[112:115], v217 offset:50336
	s_waitcnt lgkmcnt(1)
	v_mfma_f32_32x32x16_bf16 v[80:95], v[2:5], v[168:171], v[80:95]
	ds_read_b128 v[2:5], v217 offset:58912
	s_waitcnt vmcnt(0)
	ds_read_b128 v[116:119], v217 offset:59040
	s_waitcnt lgkmcnt(1)
	v_mfma_f32_32x32x16_bf16 v[96:111], v[2:5], v[168:171], v[96:111]
	ds_read_b128 v[2:5], v217 offset:50240
	ds_read_b128 v[120:123], v217 offset:50368
	s_waitcnt lgkmcnt(1)
	v_mfma_f32_32x32x16_bf16 v[80:95], v[2:5], v[164:167], v[80:95]
	ds_read_b128 v[2:5], v217 offset:58944
	ds_read_b128 v[124:127], v217 offset:59072
	s_waitcnt lgkmcnt(1)
	v_mfma_f32_32x32x16_bf16 v[96:111], v[2:5], v[164:167], v[96:111]
	ds_read_b128 v[2:5], v217 offset:50272
	ds_read_b128 v[164:167], v217 offset:50400
	s_waitcnt lgkmcnt(1)
	v_mfma_f32_32x32x16_bf16 v[80:95], v[2:5], v[148:151], v[80:95]
	ds_read_b128 v[2:5], v217 offset:58976
	ds_read_b128 v[168:171], v217 offset:59104
	s_waitcnt lgkmcnt(1)
	v_mfma_f32_32x32x16_bf16 v[96:111], v[2:5], v[148:151], v[96:111]
	v_mfma_f32_32x32x16_bf16 v[80:95], v[6:9], v[152:155], v[80:95]
	v_mfma_f32_32x32x16_bf16 v[96:111], v[10:13], v[152:155], v[96:111]
	v_mfma_f32_32x32x16_bf16 v[80:95], v[112:115], v[156:159], v[80:95]
	v_mfma_f32_32x32x16_bf16 v[96:111], v[116:119], v[156:159], v[96:111]
	v_mfma_f32_32x32x16_bf16 v[80:95], v[120:123], v[160:163], v[80:95]
	v_mfma_f32_32x32x16_bf16 v[96:111], v[124:127], v[160:163], v[96:111]
	v_mfma_f32_32x32x16_bf16 v[80:95], v[164:167], v[144:147], v[80:95]
	s_waitcnt lgkmcnt(0)
	v_mfma_f32_32x32x16_bf16 v[96:111], v[168:171], v[144:147], v[96:111]

.LBB3_60:
	s_waitcnt vmcnt(8)
	s_waitcnt vmcnt(9)
	ds_write_b128 v222, v[112:115] offset:32768
	s_waitcnt vmcnt(8)
	ds_write_b128 v222, v[116:119] offset:41472
	s_and_saveexec_b64 s[6:7], s[0:1]
	ds_write_b32 v226, v181
	s_or_b64 exec, exec, s[6:7]
	s_waitcnt lgkmcnt(0)
	ds_read_b128 v[4:7], v225
	ds_read_b128 v[8:11], v225 offset:32
	s_and_b64 s[6:7], s[12:13], exec
	s_cselect_b32 s7, s17, s31
	s_cselect_b32 s6, s16, s30
	s_waitcnt lgkmcnt(1)
	v_rcp_f32_e32 v87, v4
	v_rcp_f32_e32 v86, v5
	v_rcp_f32_e32 v85, v6
	v_rcp_f32_e32 v84, v7
	ds_read_b128 v[4:7], v225 offset:64
	ds_read_b128 v[88:91], v225 offset:96
	s_waitcnt lgkmcnt(2)
	v_rcp_f32_e32 v83, v8
	v_rcp_f32_e32 v82, v9
	v_rcp_f32_e32 v81, v10
	v_rcp_f32_e32 v80, v11
	s_waitcnt lgkmcnt(1)
	v_rcp_f32_e32 v15, v4
	v_rcp_f32_e32 v14, v5
	v_rcp_f32_e32 v13, v6
	v_rcp_f32_e32 v12, v7
	s_waitcnt lgkmcnt(0)
	v_rcp_f32_e32 v11, v88
	v_rcp_f32_e32 v10, v89
	v_rcp_f32_e32 v9, v90
	v_rcp_f32_e32 v8, v91
	s_cmp_eq_u64 s[6:7], 0
	s_cbranch_scc1 .LBB3_98
	s_and_saveexec_b64 s[14:15], s[0:1]
	s_cbranch_execz .LBB3_65
	s_and_b64 s[44:45], s[12:13], exec
	s_cselect_b32 s44, s19, s35
	s_cselect_b32 s45, s18, s34
	v_mov_b32_e32 v4, s45
	v_mov_b32_e32 v5, s44
	v_lshlrev_b32_e32 v0, 1, v0
	v_lshl_add_u64 v[4:5], v[0:1], 2, v[4:5]
	global_store_dwordx2 v[4:5], v[2:3], off

	.amdhsa_kernel _ZN4attn10attn_splitI14__hip_bfloat16S1_EEvPKT_S4_S4_PT0_PfS7_PKjPjii
		.amdhsa_group_segment_fixed_size 2304
		.amdhsa_private_segment_fixed_size 0
		.amdhsa_kernarg_size 328
		.amdhsa_user_sgpr_count 2
		.amdhsa_user_sgpr_dispatch_ptr 0
		.amdhsa_user_sgpr_queue_ptr 0
		.amdhsa_user_sgpr_kernarg_segment_ptr 1
		.amdhsa_user_sgpr_dispatch_id 0
		.amdhsa_user_sgpr_kernarg_preload_length 0
		.amdhsa_user_sgpr_kernarg_preload_offset 0
		.amdhsa_user_sgpr_private_segment_size 0
		.amdhsa_uses_dynamic_stack 0
		.amdhsa_enable_private_segment 0
		.amdhsa_system_sgpr_workgroup_id_x 1
		.amdhsa_system_sgpr_workgroup_id_y 0
		.amdhsa_system_sgpr_workgroup_id_z 0
		.amdhsa_system_sgpr_workgroup_info 0
		.amdhsa_system_vgpr_workitem_id 2
		.amdhsa_next_free_vgpr 254
		.amdhsa_next_free_sgpr 64
		.amdhsa_accum_offset 256
		.amdhsa_reserve_vcc 1
		.amdhsa_float_round_mode_32 0
		.amdhsa_float_round_mode_16_64 0
		.amdhsa_float_denorm_mode_32 3
		.amdhsa_float_denorm_mode_16_64 3
		.amdhsa_dx10_clamp 1
		.amdhsa_ieee_mode 1
		.amdhsa_fp16_overflow 0
		.amdhsa_tg_split 0
		.amdhsa_exception_fp_ieee_invalid_op 0
		.amdhsa_exception_fp_denorm_src 0
		.amdhsa_exception_fp_ieee_div_zero 0
		.amdhsa_exception_fp_ieee_overflow 0
		.amdhsa_exception_fp_ieee_underflow 0
		.amdhsa_exception_fp_ieee_inexact 0
		.amdhsa_exception_int_div_zero 0
	.end_amdhsa_kernel

amdhsa.kernels:
  - .agpr_count:     0
    .args:
      - .offset:         0
        .size:           128
        .value_kind:     by_value
      - .actual_access:  read_only
        .address_space:  global
        .offset:         128
        .size:           8
        .value_kind:     global_buffer
      - .address_space:  global
        .offset:         136
        .size:           8
        .value_kind:     global_buffer
      - .offset:         144
        .size:           64
        .value_kind:     by_value
      - .offset:         208
        .size:           4
        .value_kind:     hidden_block_count_x
      - .offset:         212
        .size:           4
        .value_kind:     hidden_block_count_y
      - .offset:         216
        .size:           4
        .value_kind:     hidden_block_count_z
      - .offset:         220
        .size:           2
        .value_kind:     hidden_group_size_x
      - .offset:         222
        .size:           2
        .value_kind:     hidden_group_size_y
      - .offset:         224
        .size:           2
        .value_kind:     hidden_group_size_z
      - .offset:         226
        .size:           2
        .value_kind:     hidden_remainder_x
      - .offset:         228
        .size:           2
        .value_kind:     hidden_remainder_y
      - .offset:         230
        .size:           2
        .value_kind:     hidden_remainder_z
      - .offset:         248
        .size:           8
        .value_kind:     hidden_global_offset_x
      - .offset:         256
        .size:           8
        .value_kind:     hidden_global_offset_y
      - .offset:         264
        .size:           8
        .value_kind:     hidden_global_offset_z
      - .offset:         272
        .size:           2
        .value_kind:     hidden_grid_dims
    .group_segment_fixed_size: 16896
    .kernarg_segment_align: 8
    .kernarg_segment_size: 464
    .language:       OpenCL C
    .language_version:
      - 2
      - 0
    .max_flat_workgroup_size: 256
    .name:           _Z11prep_kernel7CvtArgsPKiPj6LnArgs
    .private_segment_fixed_size: 0
    .sgpr_count:     60
    .sgpr_spill_count: 0
    .symbol:         _Z11prep_kernel7CvtArgsPKiPj6LnArgs.kd
    .uniform_work_group_size: 1
    .uses_dynamic_stack: false
    .vgpr_count:     120
    .vgpr_spill_count: 0
    .wavefront_size: 64
  - .agpr_count:     0
    .args:
      - .actual_access:  read_only
        .address_space:  global
        .offset:         0
        .size:           8
        .value_kind:     global_buffer
      - .actual_access:  read_only
        .address_space:  global
        .offset:         8
        .size:           8
        .value_kind:     global_buffer
      - .actual_access:  write_only
        .address_space:  global
        .offset:         16
        .size:           8
        .value_kind:     global_buffer
      - .actual_access:  read_only
        .address_space:  global
        .offset:         24
        .size:           8
        .value_kind:     global_buffer
      - .offset:         32
        .size:           4
        .value_kind:     by_value
      - .actual_access:  read_only
        .address_space:  global
        .offset:         40
        .size:           8
        .value_kind:     global_buffer
      - .actual_access:  read_only
        .address_space:  global
        .offset:         48
        .size:           8
        .value_kind:     global_buffer
      - .actual_access:  read_only
        .address_space:  global
        .offset:         56
        .size:           8
        .value_kind:     global_buffer
      - .actual_access:  read_only
        .address_space:  global
        .offset:         64
        .size:           8
        .value_kind:     global_buffer
      - .offset:         72
        .size:           4
        .value_kind:     hidden_block_count_x
      - .offset:         76
        .size:           4
        .value_kind:     hidden_block_count_y
      - .offset:         80
        .size:           4
        .value_kind:     hidden_block_count_z
      - .offset:         84
        .size:           2
        .value_kind:     hidden_group_size_x
      - .offset:         86
        .size:           2
        .value_kind:     hidden_group_size_y
      - .offset:         88
        .size:           2
        .value_kind:     hidden_group_size_z
      - .offset:         90
        .size:           2
        .value_kind:     hidden_remainder_x
      - .offset:         92
        .size:           2
        .value_kind:     hidden_remainder_y
      - .offset:         94
        .size:           2
        .value_kind:     hidden_remainder_z
      - .offset:         112
        .size:           8
        .value_kind:     hidden_global_offset_x
      - .offset:         120
        .size:           8
        .value_kind:     hidden_global_offset_y
      - .offset:         128
        .size:           8
        .value_kind:     hidden_global_offset_z
      - .offset:         136
        .size:           2
        .value_kind:     hidden_grid_dims
    .group_segment_fixed_size: 32768
    .kernarg_segment_align: 8
    .kernarg_segment_size: 328
    .language:       OpenCL C
    .language_version:
      - 2
      - 0
    .max_flat_workgroup_size: 256
    .name:           _ZN4attn12attn_combineEPKfS1_PtPKjiPKtS6_S6_PKi
    .private_segment_fixed_size: 0
    .sgpr_count:     30
    .sgpr_spill_count: 0
    .symbol:         _ZN4attn12attn_combineEPKfS1_PtPKjiPKtS6_S6_PKi.kd
    .uniform_work_group_size: 1
    .uses_dynamic_stack: false
    .vgpr_count:     62
    .vgpr_spill_count: 0
    .wavefront_size: 64
  - .agpr_count:     0
    .args:
      - .actual_access:  read_only
        .address_space:  global
        .offset:         0
        .size:           8
        .value_kind:     global_buffer
      - .actual_access:  read_only
        .address_space:  global
        .offset:         8
        .size:           8
        .value_kind:     global_buffer
      - .offset:         16
        .size:           4
        .value_kind:     by_value
      - .offset:         20
        .size:           4
        .value_kind:     by_value
      - .offset:         24
        .size:           4
        .value_kind:     by_value
      - .offset:         32
        .size:           72
        .value_kind:     by_value
    .group_segment_fixed_size: 0
    .kernarg_segment_align: 8
    .kernarg_segment_size: 104
    .language:       OpenCL C
    .language_version:
      - 2
      - 0
    .max_flat_workgroup_size: 512
    .name:           _Z6gemm4pILi96ELi2ELi0EEvPKtS1_iii7EpiArgs
    .private_segment_fixed_size: 0
    .sgpr_count:     68
    .sgpr_spill_count: 0
    .symbol:         _Z6gemm4pILi96ELi2ELi0EEvPKtS1_iii7EpiArgs.kd
    .uniform_work_group_size: 1
    .uses_dynamic_stack: false
    .vgpr_count:     216
    .vgpr_spill_count: 0
    .wavefront_size: 64
  - .agpr_count:     0
    .args:
      - .actual_access:  read_only
        .address_space:  global
        .offset:         0
        .size:           8
        .value_kind:     global_buffer
      - .actual_access:  read_only
        .address_space:  global
        .offset:         8
        .size:           8
        .value_kind:     global_buffer
      - .actual_access:  read_only
        .address_space:  global
        .offset:         16
        .size:           8
        .value_kind:     global_buffer
      - .actual_access:  write_only
        .address_space:  global
        .offset:         24
        .size:           8
        .value_kind:     global_buffer
      - .actual_access:  write_only
        .address_space:  global
        .offset:         32
        .size:           8
        .value_kind:     global_buffer
      - .actual_access:  write_only
        .address_space:  global
        .offset:         40
        .size:           8
        .value_kind:     global_buffer
      - .actual_access:  read_only
        .address_space:  global
        .offset:         48
        .size:           8
        .value_kind:     global_buffer
      - .actual_access:  write_only
        .address_space:  global
        .offset:         56
        .size:           8
        .value_kind:     global_buffer
      - .offset:         64
        .size:           4
        .value_kind:     by_value
      - .offset:         68
        .size:           4
        .value_kind:     by_value
      - .offset:         72
        .size:           4
        .value_kind:     hidden_block_count_x
      - .offset:         76
        .size:           4
        .value_kind:     hidden_block_count_y
      - .offset:         80
        .size:           4
        .value_kind:     hidden_block_count_z
      - .offset:         84
        .size:           2
        .value_kind:     hidden_group_size_x
      - .offset:         86
        .size:           2
        .value_kind:     hidden_group_size_y
      - .offset:         88
        .size:           2
        .value_kind:     hidden_group_size_z
      - .offset:         90
        .size:           2
        .value_kind:     hidden_remainder_x
      - .offset:         92
        .size:           2
        .value_kind:     hidden_remainder_y
      - .offset:         94
        .size:           2
        .value_kind:     hidden_remainder_z
      - .offset:         112
        .size:           8
        .value_kind:     hidden_global_offset_x
      - .offset:         120
        .size:           8
        .value_kind:     hidden_global_offset_y
      - .offset:         128
        .size:           8
        .value_kind:     hidden_global_offset_z
      - .offset:         136
        .size:           2
        .value_kind:     hidden_grid_dims
      - .offset:         192
        .size:           4
        .value_kind:     hidden_dynamic_lds_size
    .group_segment_fixed_size: 2304
    .kernarg_segment_align: 8
    .kernarg_segment_size: 328
    .language:       OpenCL C
    .language_version:
      - 2
      - 0
    .max_flat_workgroup_size: 512
    .name:           _ZN4attn10attn_splitI14__hip_bfloat16S1_EEvPKT_S4_S4_PT0_PfS7_PKjPjii
    .private_segment_fixed_size: 0
    .sgpr_count:     70
    .sgpr_spill_count: 0
    .symbol:         _ZN4attn10attn_splitI14__hip_bfloat16S1_EEvPKT_S4_S4_PT0_PfS7_PKjPjii.kd
    .uniform_work_group_size: 1
    .uses_dynamic_stack: false
    .vgpr_count:     254
    .vgpr_spill_count: 0
    .wavefront_size: 64
  - .agpr_count:     0
    .args:
      - .actual_access:  read_only
        .address_space:  global
        .offset:         0
        .size:           8
        .value_kind:     global_buffer
      - .actual_access:  read_only
        .address_space:  global
        .offset:         8
        .size:           8
        .value_kind:     global_buffer
      - .offset:         16
        .size:           4
        .value_kind:     by_value
      - .offset:         20
        .size:           4
        .value_kind:     by_value
      - .offset:         24
        .size:           4
        .value_kind:     by_value
      - .offset:         32
        .size:           72
        .value_kind:     by_value
    .group_segment_fixed_size: 0
    .kernarg_segment_align: 8
    .kernarg_segment_size: 104
    .language:       OpenCL C
    .language_version:
      - 2
      - 0
    .max_flat_workgroup_size: 512
    .name:           _Z6gemm4pILi64ELi2ELi3EEvPKtS1_iii7EpiArgs
    .private_segment_fixed_size: 0
    .sgpr_count:     49
    .sgpr_spill_count: 0
    .symbol:         _Z6gemm4pILi64ELi2ELi3EEvPKtS1_iii7EpiArgs.kd
    .uniform_work_group_size: 1
    .uses_dynamic_stack: false
    .vgpr_count:     194
    .vgpr_spill_count: 0
    .wavefront_size: 64
  - .agpr_count:     0
    .args:
      - .actual_access:  read_only
        .address_space:  global
        .offset:         0
        .size:           8
        .value_kind:     global_buffer
      - .actual_access:  read_only
        .address_space:  global
        .offset:         8
        .size:           8
        .value_kind:     global_buffer
      - .offset:         16
        .size:           4
        .value_kind:     by_value
      - .offset:         20
        .size:           4
        .value_kind:     by_value
      - .offset:         24
        .size:           4
        .value_kind:     by_value
      - .offset:         32
        .size:           72
        .value_kind:     by_value
    .group_segment_fixed_size: 0
    .kernarg_segment_align: 8
    .kernarg_segment_size: 104
    .language:       OpenCL C
    .language_version:
      - 2
      - 0
    .max_flat_workgroup_size: 512
    .name:           _Z6gemm4pILi96ELi2ELi4EEvPKtS1_iii7EpiArgs
    .private_segment_fixed_size: 0
    .sgpr_count:     71
    .sgpr_spill_count: 0
    .symbol:         _Z6gemm4pILi96ELi2ELi4EEvPKtS1_iii7EpiArgs.kd
    .uniform_work_group_size: 1
    .uses_dynamic_stack: false
    .vgpr_count:     244
    .vgpr_spill_count: 0
    .wavefront_size: 64
  - .agpr_count:     0
    .args:
      - .actual_access:  read_only
        .address_space:  global
        .offset:         0
        .size:           8
        .value_kind:     global_buffer
      - .actual_access:  read_only
        .address_space:  global
        .offset:         8
        .size:           8
        .value_kind:     global_buffer
      - .offset:         16
        .size:           4
        .value_kind:     by_value
      - .offset:         20
        .size:           4
        .value_kind:     by_value
      - .offset:         24
        .size:           4
        .value_kind:     by_value
      - .offset:         32
        .size:           72
        .value_kind:     by_value
    .group_segment_fixed_size: 0
    .kernarg_segment_align: 8
    .kernarg_segment_size: 104
    .language:       OpenCL C
    .language_version:
      - 2
      - 0
    .max_flat_workgroup_size: 512
    .name:           _Z6gemm4pILi64ELi2ELi1EEvPKtS1_iii7EpiArgs
    .private_segment_fixed_size: 0
    .sgpr_count:     50
    .sgpr_spill_count: 0
    .symbol:         _Z6gemm4pILi64ELi2ELi1EEvPKtS1_iii7EpiArgs.kd
    .uniform_work_group_size: 1
    .uses_dynamic_stack: false
    .vgpr_count:     186
    .vgpr_spill_count: 0
    .wavefront_size: 64
